# baseline (speedup 1.0000x reference)
.LBB2_1:
	v_mfma_f32_32x32x16_f16 v[96:111], v[172:175], v[136:139], v[0:15]
	s_mov_b32 s17, s31
	s_mov_b32 s18, s15
	v_add_u32_e32 v185, s18, v181
	ds_read_b64_tr_b16 v[176:177], v185 offset:24576
	ds_read_b64_tr_b16 v[178:179], v185 offset:25088
	v_add_f32_e32 v80, v64, v65
	v_add_f32_e32 v80, v66, v80
	v_add_f32_e32 v80, v67, v80
	v_add_f32_e32 v80, v68, v80
	v_add_f32_e32 v80, v69, v80
	v_cvt_pk_f16_f32 v140, v64, v65
	v_cvt_pk_f16_f32 v141, v66, v67
	ds_read_b64_tr_b16 v[172:173], v185 offset:28672
	ds_read_b64_tr_b16 v[174:175], v185 offset:29184
	v_add_f32_e32 v64, v70, v80
	s_waitcnt lgkmcnt(10)
	v_mfma_f32_32x32x16_f16 v[80:95], v[168:171], v[136:139], v[0:15]
	v_add_f32_e32 v64, v71, v64
	v_add_f32_e32 v64, v72, v64
	v_add_f32_e32 v64, v73, v64
	v_cvt_pk_f16_f32 v142, v68, v69
	v_cvt_pk_f16_f32 v143, v70, v71
	ds_read_b64_tr_b16 v[68:69], v185 offset:25600
	ds_read_b64_tr_b16 v[70:71], v185 offset:26112
	s_waitcnt lgkmcnt(11)
	v_mfma_f32_32x32x16_f16 v[96:111], v[164:167], v[128:131], v[96:111]
	v_add_f32_e32 v64, v74, v64
	v_add_f32_e32 v64, v75, v64
	v_add_f32_e32 v64, v76, v64
	v_add_f32_e32 v116, v77, v64
	v_cvt_pk_f16_f32 v132, v72, v73
	v_cvt_pk_f16_f32 v133, v74, v75
	ds_read_b64_tr_b16 v[64:65], v185 offset:29696
	ds_read_b64_tr_b16 v[66:67], v185 offset:30208
	s_waitcnt lgkmcnt(12)
	v_mfma_f32_32x32x16_f16 v[80:95], v[160:163], v[128:131], v[80:95]
	v_add_f32_e32 v72, v78, v116
	v_add_f32_e32 v72, v79, v72
	v_add_f32_e32 v72, v48, v72
	v_add_f32_e32 v116, v49, v72
	v_cvt_pk_f16_f32 v134, v76, v77
	v_cvt_pk_f16_f32 v135, v78, v79
	ds_read_b64_tr_b16 v[72:73], v185 offset:26624
	ds_read_b64_tr_b16 v[74:75], v185 offset:27136
	s_waitcnt lgkmcnt(13)
	v_mfma_f32_32x32x16_f16 v[96:111], v[156:159], v[120:123], v[96:111]
	v_add_f32_e32 v76, v50, v116
	v_add_f32_e32 v76, v51, v76
	v_add_f32_e32 v76, v52, v76
	v_add_f32_e32 v76, v53, v76
	v_cvt_pk_f16_f32 v124, v48, v49
	v_cvt_pk_f16_f32 v125, v50, v51
	ds_read_b64_tr_b16 v[48:49], v185 offset:30720
	ds_read_b64_tr_b16 v[50:51], v185 offset:31232
	s_waitcnt lgkmcnt(14)
	v_mfma_f32_32x32x16_f16 v[80:95], v[152:155], v[120:123], v[80:95]
	s_add_i32 m0, s14, s25
	s_nop 0
	global_load_lds_dwordx4 v180, s[44:45]
	s_add_i32 m0, s28, s26
	s_add_u32 s44, s44, 0x2000
	s_addc_u32 s45, s45, 0
	global_load_lds_dwordx4 v180, s[46:47]
	s_add_u32 s46, s46, 0x2000
	s_addc_u32 s47, s47, 0
	v_add_f32_e32 v76, v54, v76
	v_add_f32_e32 v76, v55, v76
	v_add_f32_e32 v76, v56, v76
	v_add_f32_e32 v76, v57, v76
	v_cvt_pk_f16_f32 v126, v52, v53
	v_cvt_pk_f16_f32 v127, v54, v55
	ds_read_b64_tr_b16 v[52:53], v185 offset:27648
	ds_read_b64_tr_b16 v[54:55], v185 offset:28160
	s_waitcnt lgkmcnt(14)
	v_mfma_f32_32x32x16_f16 v[96:111], v[148:151], v[112:115], v[96:111]
	v_add_f32_e32 v76, v58, v76
	v_add_f32_e32 v76, v59, v76
	v_add_f32_e32 v76, v60, v76
	v_add_f32_e32 v76, v61, v76
	v_cvt_pk_f16_f32 v116, v56, v57
	v_cvt_pk_f16_f32 v117, v58, v59
	ds_read_b64_tr_b16 v[56:57], v185 offset:31744
	ds_read_b64_tr_b16 v[58:59], v185 offset:32256
	v_mfma_f32_32x32x16_f16 v[80:95], v[144:147], v[112:115], v[80:95]
	v_add_f32_e32 v76, v62, v76
	v_add_f32_e32 v76, v63, v76
	v_cvt_pk_f16_f32 v118, v60, v61
	v_cvt_pk_f16_f32 v119, v62, v63
	v_cmp_lt_f32_e32 vcc, s36, v76
	s_nop 2
	s_cbranch_vccnz .Lmy_rare_1

.LBB2_4:
	v_mfma_f32_32x32x16_f16 v[64:79], v[60:63], v[136:139], v[0:15]
	v_add_u32_e32 v185, s17, v181
	ds_read_b64_tr_b16 v[144:145], v185 offset:24576
	ds_read_b64_tr_b16 v[146:147], v185 offset:25088
	v_add_f32_e32 v48, v96, v97
	v_add_f32_e32 v48, v98, v48
	v_add_f32_e32 v48, v99, v48
	v_add_f32_e32 v48, v100, v48
	v_add_f32_e32 v48, v101, v48
	v_cvt_pk_f16_f32 v140, v96, v97
	v_cvt_pk_f16_f32 v141, v98, v99
	ds_read_b64_tr_b16 v[152:153], v185 offset:28672
	ds_read_b64_tr_b16 v[154:155], v185 offset:29184
	v_add_f32_e32 v48, v102, v48
	v_add_f32_e32 v48, v103, v48
	v_add_f32_e32 v48, v104, v48
	v_add_f32_e32 v96, v105, v48
	s_waitcnt lgkmcnt(10)
	v_mfma_f32_32x32x16_f16 v[48:63], v[148:151], v[136:139], v[0:15]
	v_cvt_pk_f16_f32 v142, v100, v101
	v_cvt_pk_f16_f32 v143, v102, v103
	ds_read_b64_tr_b16 v[148:149], v185 offset:25600
	ds_read_b64_tr_b16 v[150:151], v185 offset:26112
	s_waitcnt lgkmcnt(11)
	v_mfma_f32_32x32x16_f16 v[64:79], v[176:179], v[128:131], v[64:79]
	v_add_f32_e32 v96, v106, v96
	v_add_f32_e32 v96, v107, v96
	v_add_f32_e32 v96, v108, v96
	v_add_f32_e32 v96, v109, v96
	v_cvt_pk_f16_f32 v132, v104, v105
	v_cvt_pk_f16_f32 v133, v106, v107
	ds_read_b64_tr_b16 v[100:101], v185 offset:29696
	ds_read_b64_tr_b16 v[102:103], v185 offset:30208
	s_waitcnt lgkmcnt(12)
	v_mfma_f32_32x32x16_f16 v[48:63], v[172:175], v[128:131], v[48:63]
	v_add_f32_e32 v96, v110, v96
	v_add_f32_e32 v96, v111, v96
	v_add_f32_e32 v96, v80, v96
	v_add_f32_e32 v104, v81, v96
	v_cvt_pk_f16_f32 v134, v108, v109
	v_cvt_pk_f16_f32 v135, v110, v111
	ds_read_b64_tr_b16 v[96:97], v185 offset:26624
	ds_read_b64_tr_b16 v[98:99], v185 offset:27136
	s_waitcnt lgkmcnt(13)
	v_mfma_f32_32x32x16_f16 v[64:79], v[168:171], v[120:123], v[64:79]
	v_add_f32_e32 v104, v82, v104
	v_add_f32_e32 v104, v83, v104
	v_add_f32_e32 v104, v84, v104
	v_add_f32_e32 v104, v85, v104
	v_cvt_pk_f16_f32 v124, v80, v81
	v_cvt_pk_f16_f32 v125, v82, v83
	ds_read_b64_tr_b16 v[80:81], v185 offset:30720
	ds_read_b64_tr_b16 v[82:83], v185 offset:31232
	s_waitcnt lgkmcnt(14)
	v_mfma_f32_32x32x16_f16 v[48:63], v[164:167], v[120:123], v[48:63]
	s_add_i32 m0, s19, s25
	s_nop 0
	global_load_lds_dwordx4 v180, s[44:45]
	s_add_i32 m0, s18, s26
	s_add_u32 s44, s44, 0x2000
	s_addc_u32 s45, s45, 0
	global_load_lds_dwordx4 v180, s[46:47]
	s_add_u32 s46, s46, 0x2000
	s_addc_u32 s47, s47, 0
	v_add_f32_e32 v104, v86, v104
	v_add_f32_e32 v104, v87, v104
	v_add_f32_e32 v104, v88, v104
	v_add_f32_e32 v104, v89, v104
	v_cvt_pk_f16_f32 v126, v84, v85
	v_cvt_pk_f16_f32 v127, v86, v87
	ds_read_b64_tr_b16 v[84:85], v185 offset:27648
	ds_read_b64_tr_b16 v[86:87], v185 offset:28160
	s_waitcnt lgkmcnt(14)
	v_mfma_f32_32x32x16_f16 v[64:79], v[160:163], v[112:115], v[64:79]
	v_add_f32_e32 v104, v90, v104
	v_add_f32_e32 v104, v91, v104
	v_add_f32_e32 v104, v92, v104
	v_add_f32_e32 v104, v93, v104
	v_cvt_pk_f16_f32 v116, v88, v89
	v_cvt_pk_f16_f32 v117, v90, v91
	ds_read_b64_tr_b16 v[88:89], v185 offset:31744
	ds_read_b64_tr_b16 v[90:91], v185 offset:32256
	v_mfma_f32_32x32x16_f16 v[48:63], v[156:159], v[112:115], v[48:63]
	v_add_f32_e32 v104, v94, v104
	v_add_f32_e32 v104, v95, v104
	v_cvt_pk_f16_f32 v118, v92, v93
	v_cvt_pk_f16_f32 v119, v94, v95
	v_cmp_lt_f32_e32 vcc, s36, v104
	s_nop 2
	s_cbranch_vccnz .Lmy_rare_2
